# v27 + batched candidate-score loads in block selection + layer-1 weight conversion at one of eight seams
# baseline (speedup 1.0000x reference)
; #define LAS __attribute__((address_space(3)))
; __device__ __forceinline__ void ph_attn_fast2(const Args& a, LAS unsigned char* lds) {
;     ...
;                     const LAS _Float16* pst = ps + (4 * rnd + tl) * 512;
;                     float v[8];
; #pragma unroll
;                     for (int k = 0; k < 8; ++k) { const int j = li + 16 * k;
;                         float x;
;                         if (j > cur) x = NEG;
;                         else if (j == 0 || j == cur || j == cur - 1) x = NEG;
;                         else { const int n0 = 4 * j; x = (float)pst[n0 - 1] + 2.0f * ((float)pst[n0] + (float)pst[n0 + 1] + (float)pst[n0 + 2]) + (float)pst[n0 + 3]; }
;                         v[k] = x; }
.LBB0_1983:
	v_or_b32_e32 v1, s31, v212
	v_lshl_add_u32 v4, v1, 10, s37
	v_add_u32_e32 v26, v4, v227
	v_add_u32_e32 v27, v4, v229
	v_add_u32_e32 v28, v4, v231
	v_add_u32_e32 v29, v4, v233
	v_add_u32_e32 v30, v4, v235
	v_add_u32_e32 v31, v4, v237
	v_add_u32_e32 v32, v4, v239
	v_add_u32_e32 v33, v4, v241
	v_add_u32_e32 v34, -2, v26
	v_add_u32_e32 v35, -2, v27
	v_add_u32_e32 v36, -2, v28
	v_add_u32_e32 v37, -2, v29
	v_add_u32_e32 v38, -2, v30
	v_add_u32_e32 v39, -2, v31
	v_add_u32_e32 v40, -2, v32
	v_add_u32_e32 v41, -2, v33
	ds_read_b64 v[42:43], v34
	ds_read_b64 v[44:45], v35
	ds_read_b64 v[46:47], v36
	ds_read_b64 v[48:49], v37
	ds_read_b64 v[50:51], v38
	ds_read_b64 v[52:53], v39
	ds_read_b64 v[54:55], v40
	ds_read_b64 v[56:57], v41
	ds_read_u16 v58, v26 offset:6
	ds_read_u16 v59, v27 offset:6
	ds_read_u16 v60, v28 offset:6
	ds_read_u16 v61, v29 offset:6
	s_waitcnt lgkmcnt(0)
	ds_read_u16 v78, v30 offset:6
	ds_read_u16 v79, v31 offset:6
	ds_read_u16 v80, v32 offset:6
	ds_read_u16 v81, v33 offset:6
	v_cvt_f32_f16_e32 v62, v43
	v_cvt_f32_f16_sdwa v63, v42 dst_sel:DWORD dst_unused:UNUSED_PAD src0_sel:WORD_1
	v_cvt_f32_f16_sdwa v43, v43 dst_sel:DWORD dst_unused:UNUSED_PAD src0_sel:WORD_1
	v_cvt_f32_f16_e32 v58, v58
	v_add_f32_e32 v62, v62, v63
	v_add_f32_e32 v62, v62, v43
	v_fma_mix_f32 v62, v62, s39, v42 op_sel_hi:[0,0,1]
	v_add_f32_e32 v62, v62, v58
	v_cndmask_b32_e64 v11, v246, v62, s[4:5]
	v_cvt_f32_f16_e32 v64, v45
	v_cvt_f32_f16_sdwa v65, v44 dst_sel:DWORD dst_unused:UNUSED_PAD src0_sel:WORD_1
	v_cvt_f32_f16_sdwa v45, v45 dst_sel:DWORD dst_unused:UNUSED_PAD src0_sel:WORD_1
	v_cvt_f32_f16_e32 v59, v59
	v_add_f32_e32 v64, v64, v65
	v_add_f32_e32 v64, v64, v45
	v_fma_mix_f32 v64, v64, s39, v44 op_sel_hi:[0,0,1]
	v_add_f32_e32 v64, v64, v59
	v_cndmask_b32_e64 v2, v246, v64, s[6:7]
	v_cvt_f32_f16_e32 v66, v47
	v_cvt_f32_f16_sdwa v67, v46 dst_sel:DWORD dst_unused:UNUSED_PAD src0_sel:WORD_1
	v_cvt_f32_f16_sdwa v47, v47 dst_sel:DWORD dst_unused:UNUSED_PAD src0_sel:WORD_1
	v_cvt_f32_f16_e32 v60, v60
	v_add_f32_e32 v66, v66, v67
	v_add_f32_e32 v66, v66, v47
	v_fma_mix_f32 v66, v66, s39, v46 op_sel_hi:[0,0,1]
	v_add_f32_e32 v66, v66, v60
	v_cndmask_b32_e64 v14, v246, v66, s[18:19]
	v_cvt_f32_f16_e32 v68, v49
	v_cvt_f32_f16_sdwa v69, v48 dst_sel:DWORD dst_unused:UNUSED_PAD src0_sel:WORD_1
	v_cvt_f32_f16_sdwa v49, v49 dst_sel:DWORD dst_unused:UNUSED_PAD src0_sel:WORD_1
	v_cvt_f32_f16_e32 v61, v61
	v_add_f32_e32 v68, v68, v69
	v_add_f32_e32 v68, v68, v49
	v_fma_mix_f32 v68, v68, s39, v48 op_sel_hi:[0,0,1]
	v_add_f32_e32 v68, v68, v61
	v_cndmask_b32_e64 v12, v246, v68, s[10:11]
	s_waitcnt lgkmcnt(0)
	v_cvt_f32_f16_e32 v70, v51
	v_cvt_f32_f16_sdwa v71, v50 dst_sel:DWORD dst_unused:UNUSED_PAD src0_sel:WORD_1
	v_cvt_f32_f16_sdwa v51, v51 dst_sel:DWORD dst_unused:UNUSED_PAD src0_sel:WORD_1
	v_cvt_f32_f16_e32 v78, v78
	v_add_f32_e32 v70, v70, v71
	v_add_f32_e32 v70, v70, v51
	v_fma_mix_f32 v70, v70, s39, v50 op_sel_hi:[0,0,1]
	v_add_f32_e32 v70, v70, v78
	v_cndmask_b32_e64 v16, v246, v70, s[12:13]
	v_cvt_f32_f16_e32 v72, v53
	v_cvt_f32_f16_sdwa v73, v52 dst_sel:DWORD dst_unused:UNUSED_PAD src0_sel:WORD_1
	v_cvt_f32_f16_sdwa v53, v53 dst_sel:DWORD dst_unused:UNUSED_PAD src0_sel:WORD_1
	v_cvt_f32_f16_e32 v79, v79
	v_add_f32_e32 v72, v72, v73
	v_add_f32_e32 v72, v72, v53
	v_fma_mix_f32 v72, v72, s39, v52 op_sel_hi:[0,0,1]
	v_add_f32_e32 v72, v72, v79
	v_cndmask_b32_e64 v15, v246, v72, s[14:15]
	v_cvt_f32_f16_e32 v74, v55
	v_cvt_f32_f16_sdwa v75, v54 dst_sel:DWORD dst_unused:UNUSED_PAD src0_sel:WORD_1
	v_cvt_f32_f16_sdwa v55, v55 dst_sel:DWORD dst_unused:UNUSED_PAD src0_sel:WORD_1
	v_cvt_f32_f16_e32 v80, v80
	v_add_f32_e32 v74, v74, v75
	v_add_f32_e32 v74, v74, v55
	v_fma_mix_f32 v74, v74, s39, v54 op_sel_hi:[0,0,1]
	v_add_f32_e32 v74, v74, v80
	v_cndmask_b32_e64 v18, v246, v74, s[0:1]
	v_cvt_f32_f16_e32 v76, v57
	v_cvt_f32_f16_sdwa v77, v56 dst_sel:DWORD dst_unused:UNUSED_PAD src0_sel:WORD_1
	v_cvt_f32_f16_sdwa v57, v57 dst_sel:DWORD dst_unused:UNUSED_PAD src0_sel:WORD_1
	v_cvt_f32_f16_e32 v81, v81
	v_add_f32_e32 v76, v76, v77
	v_add_f32_e32 v76, v76, v57
	v_fma_mix_f32 v76, v76, s39, v56 op_sel_hi:[0,0,1]
	v_add_f32_e32 v76, v76, v81
	v_cndmask_b32_e64 v17, v246, v76, s[8:9]
	s_andn2_b64 vcc, exec, s[22:23]
	v_mov_b64_e32 v[4:5], s[16:17]
	v_mov_b32_e32 v13, s29
	v_mov_b32_e32 v10, s28
	s_cbranch_vccnz .LBB0_2004
	s_mov_b32 s26, 0
	v_mov_b32_e32 v13, s29
	v_mov_b32_e32 v10, s28
	v_mov_b64_e32 v[4:5], s[16:17]
	s_branch .LBB0_2002

; #define LAS __attribute__((address_space(3)))
;     __device__ __forceinline__ bool next(int i, pg8::Unit& u) const { const int L = i * G + c; if (L >= 256) return false; u.pm = L >> 1; u.pn = L & 1; u.ord = i; return true; }
;     __device__ __forceinline__ bool next(int i, pg8::Unit& u) const { const int L = i * G + c; if (L >= 64) return false; u.pm = L >> 1; u.pn = L & 1; u.ord = i; return true; }
; __device__ __forceinline__ void cvt1_run(const Args& a, int& next, int stride, int quota, LAS float* scr, int lane) {
; #pragma unroll 1
;     for (int q = 0; q < quota && next < CVT1_ITEMS; ++q) {
; __device__ __forceinline__ void ph_attn_fast2(const Args& a, LAS unsigned char* lds) {
;     ...
;             if ((seam >> 1) == (int)(blockIdx.x & 3u)) cvt1_run(a, cvt_next, cvt_stride, 6, cvt_scr, lane);
;             ++seam;
.LBB0_2183:
	v_readlane_b32 s3, v252, 6
	s_and_b32 s3, s3, 7
	s_cmp_eq_u32 s70, s3
	s_cselect_b64 s[2:3], -1, 0
	s_cmp_lt_i32 s25, 0x18180
	s_cselect_b64 s[4:5], -1, 0
	s_and_b64 s[2:3], s[2:3], s[4:5]
	s_andn2_b64 vcc, exec, s[2:3]
	s_cbranch_vccnz .LBB0_2233
	s_lshl_b32 s54, s25, 5
	s_lshl_b32 s55, s66, 5
	s_mov_b32 s56, 0

; #define LAS __attribute__((address_space(3)))
;     __device__ __forceinline__ bool next(int i, pg8::Unit& u) const { const int L = i * G + c; if (L >= 256) return false; u.pm = L >> 1; u.pn = L & 1; u.ord = i; return true; }
;     __device__ __forceinline__ bool next(int i, pg8::Unit& u) const { const int L = i * G + c; if (L >= 64) return false; u.pm = L >> 1; u.pn = L & 1; u.ord = i; return true; }
; __device__ __forceinline__ void cvt1_run(const Args& a, int& next, int stride, int quota, LAS float* scr, int lane) {
; #pragma unroll 1
;     for (int q = 0; q < quota && next < CVT1_ITEMS; ++q) {
;         CvtItem t[4]; f32x4 v[4][8]; bool ok[4];
; #pragma unroll
;         for (int u = 0; u < 4; ++u) { const int idx = next + u * stride; ok[u] = idx < CVT1_ITEMS; t[u] = cvt1_item(a, ok[u] ? idx : 0); if (ok[u]) cvt32_load(t[u], lane, v[u]); }
;         next += 4 * stride;
; #pragma unroll
;         for (int u = 0; u < 4; ++u) if (ok[u]) cvt32_finish(t[u], lane, v[u], scr);
;     }
; }
.LBB0_2229:
	s_add_i32 s25, s25, s66
	s_add_i32 s2, s56, 1
	s_cmp_lt_u32 s56, 11
	s_cselect_b64 s[4:5], -1, 0
	s_cmp_lt_i32 s25, 0x18180
	s_cselect_b64 s[6:7], -1, 0
	s_and_b64 s[4:5], s[4:5], s[6:7]
	s_add_i32 s54, s54, s55
	s_and_b64 vcc, exec, s[4:5]
	s_cbranch_vccz .LBB0_2233
	s_mov_b32 s56, s2
	s_branch .LBB0_2185
